# v66 variant: XCD leaders issue the invalidate before (concurrently with) the L2 write-back instead of after its wait
# baseline (speedup 1.0000x reference)
; __device__ __forceinline__ unsigned xb_ld(unsigned* p)              { return __hip_atomic_load(p, __ATOMIC_RELAXED, __HIP_MEMORY_SCOPE_AGENT); }
; __device__ __forceinline__ unsigned xb_add(unsigned* p, unsigned v) { return __hip_atomic_fetch_add(p, v, __ATOMIC_RELAXED, __HIP_MEMORY_SCOPE_AGENT); }
; #define XB_SPIN(cond, bar) do { unsigned _sp = 0; while (cond) { __builtin_amdgcn_s_sleep(1); \
;     if ((++_sp & 255u) == 0u) { if (xb_ld(&(bar)[XB_TMO])) break; if (_sp > XB_SPIN_CAP) { atomicAdd(&(bar)[XB_TMO], 1u); break; } } } } while (0)
; __device__ __forceinline__ void xcd_barrier(const XcdBarrier& b) {
;     ...
;         if (old + 1u == (gen + 1u) * nloc) {
;             __builtin_amdgcn_fence(__ATOMIC_RELEASE, "agent");
;             asm volatile("s_waitcnt vmcnt(0)" ::: "memory");
;             const unsigned og = xb_add(&bar[XB_TOP], 1u);
;             const unsigned tg = og / nx;
;             if (og + 1u == (tg + 1u) * nx) xb_add(&bar[XB_TOPGEN], 1u);
;             else XB_SPIN(xb_ld(&bar[XB_TOPGEN]) == tg, bar);
;             __builtin_amdgcn_fence(__ATOMIC_ACQUIRE, "agent");
.LBB0_175:
	s_andn2_saveexec_b64 s[0:1], s[0:1]
	s_cbranch_execz .LBB0_191
	v_mov_b32_e32 v3, s36
	v_add_co_u32_e32 v4, vcc, 0x7000, v3
	v_mov_b32_e32 v3, s37
	buffer_inv sc1
	buffer_wbl2 sc1
	s_waitcnt vmcnt(0)
	v_addc_co_u32_e32 v5, vcc, 0, v3, vcc
	v_mov_b32_e32 v3, 1
	flat_atomic_add v3, v[4:5], v3 offset:1024 sc0
	v_cvt_f32_u32_e32 v4, v2
	v_sub_u32_e32 v5, 0, v2
	s_add_u32 s0, s36, 0x7500
	s_addc_u32 s1, s37, 0
	v_rcp_iflag_f32_e32 v4, v4
	s_mov_b64 s[6:7], -1
	v_mul_f32_e32 v4, 0x4f7ffffe, v4
	v_cvt_u32_f32_e32 v4, v4
	v_mul_lo_u32 v5, v5, v4
	v_mul_hi_u32 v5, v4, v5
	v_add_u32_e32 v4, v4, v5
	s_waitcnt vmcnt(0) lgkmcnt(0)
	v_mul_hi_u32 v4, v3, v4
	v_mul_lo_u32 v6, v4, v2
	v_add_u32_e32 v5, 1, v3
	v_sub_u32_e32 v3, v3, v6
	v_add_u32_e32 v7, 1, v4
	v_cmp_ge_u32_e32 vcc, v3, v2
	v_sub_u32_e32 v6, v3, v2
	s_nop 0
	v_cndmask_b32_e32 v4, v4, v7, vcc
	v_cndmask_b32_e32 v3, v3, v6, vcc
	v_add_u32_e32 v6, 1, v4
	v_cmp_ge_u32_e32 vcc, v3, v2
	s_nop 1
	v_cndmask_b32_e32 v4, v4, v6, vcc
	v_mad_u64_u32 v[2:3], s[4:5], v2, v4, v[2:3]
	v_cmp_ne_u32_e32 vcc, v5, v2
	v_mov_b64_e32 v[2:3], s[0:1]
	s_and_saveexec_b64 s[4:5], vcc
	s_cbranch_execz .LBB0_188
	v_mov_b64_e32 v[2:3], s[0:1]
	flat_load_dword v2, v[2:3] sc1
	s_mov_b64 s[10:11], 0
	s_waitcnt vmcnt(0) lgkmcnt(0)
	v_cmp_eq_u32_e32 vcc, v2, v4
	s_and_saveexec_b64 s[8:9], vcc
	s_cbranch_execz .LBB0_187
	s_add_u32 s6, s36, 0x4200
	s_addc_u32 s7, s37, 0
	s_mov_b32 s22, 1
	s_branch .LBB0_180
